# v9 + P2 copy slots staggered: the two B-tile columns of each (half,XCD) group convert one unit apart (8 WGs per XCD link at a time instead of 16)
# baseline (speedup 1.0000x reference)
.LBB0_196:
	s_ashr_i32 s5, s90, 4
	s_and_b32 s5, s5, -8
	s_and_b32 s6, s90, 7
	s_or_b32 s5, s5, s6
	s_mul_i32 s4, s4, s5
	s_ashr_i32 s5, s4, 31
	s_lshr_b32 s5, s5, 28
	s_add_i32 s4, s4, s5
	s_ashr_i32 s42, s4, 4
	s_bfe_u32 s5, s90, 0x10006
	s_lshr_b32 s6, s90, 7
	s_lshl_b32 s6, s6, 1
	s_sub_i32 s6, 1, s6
	s_mul_i32 s5, s5, s6
	s_add_i32 s42, s42, s5
